# INPROJ gate epilogue rewritten by hand: packed f32 mul/add/fma (same op chain, f32), u8 codes inserted with SDWA byte writes
# speedup vs baseline: 1.0038x; 1.0038x over previous
.LBB0_95:
	v_mov_b32_e32 v160, 0xbfb8aa3b
	v_mov_b32_e32 v161, 0xbfb8aa3b
	v_mov_b32_e32 v162, s92
	v_mov_b32_e32 v163, s92
	v_mov_b32_e32 v164, 0.5
	v_mov_b32_e32 v165, 0.5
	v_mul_u32_u24_e32 v140, 0x1800, v149
	v_add3_u32 v140, v140, v146, s27
	v_pk_mul_f32 v[122:123], v[122:123], v[160:161]
	v_pk_mul_f32 v[124:125], v[124:125], v[160:161]
	v_pk_mul_f32 v[126:127], v[126:127], v[160:161]
	v_pk_mul_f32 v[128:129], v[128:129], v[160:161]
	v_pk_mul_f32 v[118:119], v[118:119], v[160:161]
	v_pk_mul_f32 v[120:121], v[120:121], v[160:161]
	v_pk_mul_f32 v[114:115], v[114:115], v[160:161]
	v_pk_mul_f32 v[116:117], v[116:117], v[160:161]
	v_exp_f32_e32 v122, v122
	v_exp_f32_e32 v123, v123
	v_exp_f32_e32 v124, v124
	v_exp_f32_e32 v125, v125
	v_exp_f32_e32 v126, v126
	v_exp_f32_e32 v127, v127
	v_exp_f32_e32 v128, v128
	v_exp_f32_e32 v129, v129
	v_exp_f32_e32 v118, v118
	v_exp_f32_e32 v119, v119
	v_exp_f32_e32 v120, v120
	v_exp_f32_e32 v121, v121
	v_exp_f32_e32 v114, v114
	v_exp_f32_e32 v115, v115
	v_exp_f32_e32 v116, v116
	v_exp_f32_e32 v117, v117
	v_pk_add_f32 v[122:123], v[122:123], 1.0 op_sel_hi:[1,0]
	v_pk_add_f32 v[124:125], v[124:125], 1.0 op_sel_hi:[1,0]
	v_pk_add_f32 v[126:127], v[126:127], 1.0 op_sel_hi:[1,0]
	v_pk_add_f32 v[128:129], v[128:129], 1.0 op_sel_hi:[1,0]
	v_pk_add_f32 v[118:119], v[118:119], 1.0 op_sel_hi:[1,0]
	v_pk_add_f32 v[120:121], v[120:121], 1.0 op_sel_hi:[1,0]
	v_pk_add_f32 v[114:115], v[114:115], 1.0 op_sel_hi:[1,0]
	v_pk_add_f32 v[116:117], v[116:117], 1.0 op_sel_hi:[1,0]
	v_rcp_f32_e32 v122, v122
	v_rcp_f32_e32 v123, v123
	v_rcp_f32_e32 v124, v124
	v_rcp_f32_e32 v125, v125
	v_rcp_f32_e32 v126, v126
	v_rcp_f32_e32 v127, v127
	v_rcp_f32_e32 v128, v128
	v_rcp_f32_e32 v129, v129
	v_rcp_f32_e32 v118, v118
	v_rcp_f32_e32 v119, v119
	v_rcp_f32_e32 v120, v120
	v_rcp_f32_e32 v121, v121
	v_rcp_f32_e32 v114, v114
	v_rcp_f32_e32 v115, v115
	v_rcp_f32_e32 v116, v116
	v_rcp_f32_e32 v117, v117
	v_pk_fma_f32 v[122:123], v[122:123], v[162:163], v[164:165]
	v_pk_fma_f32 v[124:125], v[124:125], v[162:163], v[164:165]
	v_pk_fma_f32 v[126:127], v[126:127], v[162:163], v[164:165]
	v_pk_fma_f32 v[128:129], v[128:129], v[162:163], v[164:165]
	v_pk_fma_f32 v[118:119], v[118:119], v[162:163], v[164:165]
	v_pk_fma_f32 v[120:121], v[120:121], v[162:163], v[164:165]
	v_pk_fma_f32 v[114:115], v[114:115], v[162:163], v[164:165]
	v_pk_fma_f32 v[116:117], v[116:117], v[162:163], v[164:165]
	v_max_f32_e32 v122, 1.0, v122
	v_max_f32_e32 v123, 1.0, v123
	v_max_f32_e32 v124, 1.0, v124
	v_max_f32_e32 v125, 1.0, v125
	v_max_f32_e32 v126, 1.0, v126
	v_max_f32_e32 v127, 1.0, v127
	v_max_f32_e32 v128, 1.0, v128
	v_max_f32_e32 v129, 1.0, v129
	v_max_f32_e32 v118, 1.0, v118
	v_max_f32_e32 v119, 1.0, v119
	v_max_f32_e32 v120, 1.0, v120
	v_max_f32_e32 v121, 1.0, v121
	v_max_f32_e32 v114, 1.0, v114
	v_max_f32_e32 v115, 1.0, v115
	v_max_f32_e32 v116, 1.0, v116
	v_max_f32_e32 v117, 1.0, v117
	v_cvt_u32_f32_e32 v154, v122
	v_cvt_u32_f32_e32 v155, v126
	v_cvt_u32_f32_e32 v156, v118
	v_cvt_u32_f32_e32 v157, v114
	v_cvt_u32_f32_sdwa v154, v123 dst_sel:BYTE_1 dst_unused:UNUSED_PRESERVE src0_sel:DWORD
	v_cvt_u32_f32_sdwa v155, v127 dst_sel:BYTE_1 dst_unused:UNUSED_PRESERVE src0_sel:DWORD
	v_cvt_u32_f32_sdwa v156, v119 dst_sel:BYTE_1 dst_unused:UNUSED_PRESERVE src0_sel:DWORD
	v_cvt_u32_f32_sdwa v157, v115 dst_sel:BYTE_1 dst_unused:UNUSED_PRESERVE src0_sel:DWORD
	v_cvt_u32_f32_sdwa v154, v124 dst_sel:BYTE_2 dst_unused:UNUSED_PRESERVE src0_sel:DWORD
	v_cvt_u32_f32_sdwa v155, v128 dst_sel:BYTE_2 dst_unused:UNUSED_PRESERVE src0_sel:DWORD
	v_cvt_u32_f32_sdwa v156, v120 dst_sel:BYTE_2 dst_unused:UNUSED_PRESERVE src0_sel:DWORD
	v_cvt_u32_f32_sdwa v157, v116 dst_sel:BYTE_2 dst_unused:UNUSED_PRESERVE src0_sel:DWORD
	v_cvt_u32_f32_sdwa v154, v125 dst_sel:BYTE_3 dst_unused:UNUSED_PRESERVE src0_sel:DWORD
	v_cvt_u32_f32_sdwa v155, v129 dst_sel:BYTE_3 dst_unused:UNUSED_PRESERVE src0_sel:DWORD
	v_cvt_u32_f32_sdwa v156, v121 dst_sel:BYTE_3 dst_unused:UNUSED_PRESERVE src0_sel:DWORD
	v_cvt_u32_f32_sdwa v157, v117 dst_sel:BYTE_3 dst_unused:UNUSED_PRESERVE src0_sel:DWORD
	v_mov_b32_e32 v142, v140
	global_store_dwordx4 v142, v[154:157], s[20:21]
	v_pk_mul_f32 v[110:111], v[110:111], v[160:161]
	v_pk_mul_f32 v[112:113], v[112:113], v[160:161]
	v_pk_mul_f32 v[106:107], v[106:107], v[160:161]
	v_pk_mul_f32 v[108:109], v[108:109], v[160:161]
	v_pk_mul_f32 v[102:103], v[102:103], v[160:161]
	v_pk_mul_f32 v[104:105], v[104:105], v[160:161]
	v_pk_mul_f32 v[98:99], v[98:99], v[160:161]
	v_pk_mul_f32 v[100:101], v[100:101], v[160:161]
	v_exp_f32_e32 v110, v110
	v_exp_f32_e32 v111, v111
	v_exp_f32_e32 v112, v112
	v_exp_f32_e32 v113, v113
	v_exp_f32_e32 v106, v106
	v_exp_f32_e32 v107, v107
	v_exp_f32_e32 v108, v108
	v_exp_f32_e32 v109, v109
	v_exp_f32_e32 v102, v102
	v_exp_f32_e32 v103, v103
	v_exp_f32_e32 v104, v104
	v_exp_f32_e32 v105, v105
	v_exp_f32_e32 v98, v98
	v_exp_f32_e32 v99, v99
	v_exp_f32_e32 v100, v100
	v_exp_f32_e32 v101, v101
	v_pk_add_f32 v[110:111], v[110:111], 1.0 op_sel_hi:[1,0]
	v_pk_add_f32 v[112:113], v[112:113], 1.0 op_sel_hi:[1,0]
	v_pk_add_f32 v[106:107], v[106:107], 1.0 op_sel_hi:[1,0]
	v_pk_add_f32 v[108:109], v[108:109], 1.0 op_sel_hi:[1,0]
	v_pk_add_f32 v[102:103], v[102:103], 1.0 op_sel_hi:[1,0]
	v_pk_add_f32 v[104:105], v[104:105], 1.0 op_sel_hi:[1,0]
	v_pk_add_f32 v[98:99], v[98:99], 1.0 op_sel_hi:[1,0]
	v_pk_add_f32 v[100:101], v[100:101], 1.0 op_sel_hi:[1,0]
	v_rcp_f32_e32 v110, v110
	v_rcp_f32_e32 v111, v111
	v_rcp_f32_e32 v112, v112
	v_rcp_f32_e32 v113, v113
	v_rcp_f32_e32 v106, v106
	v_rcp_f32_e32 v107, v107
	v_rcp_f32_e32 v108, v108
	v_rcp_f32_e32 v109, v109
	v_rcp_f32_e32 v102, v102
	v_rcp_f32_e32 v103, v103
	v_rcp_f32_e32 v104, v104
	v_rcp_f32_e32 v105, v105
	v_rcp_f32_e32 v98, v98
	v_rcp_f32_e32 v99, v99
	v_rcp_f32_e32 v100, v100
	v_rcp_f32_e32 v101, v101
	v_pk_fma_f32 v[110:111], v[110:111], v[162:163], v[164:165]
	v_pk_fma_f32 v[112:113], v[112:113], v[162:163], v[164:165]
	v_pk_fma_f32 v[106:107], v[106:107], v[162:163], v[164:165]
	v_pk_fma_f32 v[108:109], v[108:109], v[162:163], v[164:165]
	v_pk_fma_f32 v[102:103], v[102:103], v[162:163], v[164:165]
	v_pk_fma_f32 v[104:105], v[104:105], v[162:163], v[164:165]
	v_pk_fma_f32 v[98:99], v[98:99], v[162:163], v[164:165]
	v_pk_fma_f32 v[100:101], v[100:101], v[162:163], v[164:165]
	v_max_f32_e32 v110, 1.0, v110
	v_max_f32_e32 v111, 1.0, v111
	v_max_f32_e32 v112, 1.0, v112
	v_max_f32_e32 v113, 1.0, v113
	v_max_f32_e32 v106, 1.0, v106
	v_max_f32_e32 v107, 1.0, v107
	v_max_f32_e32 v108, 1.0, v108
	v_max_f32_e32 v109, 1.0, v109
	v_max_f32_e32 v102, 1.0, v102
	v_max_f32_e32 v103, 1.0, v103
	v_max_f32_e32 v104, 1.0, v104
	v_max_f32_e32 v105, 1.0, v105
	v_max_f32_e32 v98, 1.0, v98
	v_max_f32_e32 v99, 1.0, v99
	v_max_f32_e32 v100, 1.0, v100
	v_max_f32_e32 v101, 1.0, v101
	v_cvt_u32_f32_e32 v166, v110
	v_cvt_u32_f32_e32 v167, v106
	v_cvt_u32_f32_e32 v168, v102
	v_cvt_u32_f32_e32 v169, v98
	v_cvt_u32_f32_sdwa v166, v111 dst_sel:BYTE_1 dst_unused:UNUSED_PRESERVE src0_sel:DWORD
	v_cvt_u32_f32_sdwa v167, v107 dst_sel:BYTE_1 dst_unused:UNUSED_PRESERVE src0_sel:DWORD
	v_cvt_u32_f32_sdwa v168, v103 dst_sel:BYTE_1 dst_unused:UNUSED_PRESERVE src0_sel:DWORD
	v_cvt_u32_f32_sdwa v169, v99 dst_sel:BYTE_1 dst_unused:UNUSED_PRESERVE src0_sel:DWORD
	v_cvt_u32_f32_sdwa v166, v112 dst_sel:BYTE_2 dst_unused:UNUSED_PRESERVE src0_sel:DWORD
	v_cvt_u32_f32_sdwa v167, v108 dst_sel:BYTE_2 dst_unused:UNUSED_PRESERVE src0_sel:DWORD
	v_cvt_u32_f32_sdwa v168, v104 dst_sel:BYTE_2 dst_unused:UNUSED_PRESERVE src0_sel:DWORD
	v_cvt_u32_f32_sdwa v169, v100 dst_sel:BYTE_2 dst_unused:UNUSED_PRESERVE src0_sel:DWORD
	v_cvt_u32_f32_sdwa v166, v113 dst_sel:BYTE_3 dst_unused:UNUSED_PRESERVE src0_sel:DWORD
	v_cvt_u32_f32_sdwa v167, v109 dst_sel:BYTE_3 dst_unused:UNUSED_PRESERVE src0_sel:DWORD
	v_cvt_u32_f32_sdwa v168, v105 dst_sel:BYTE_3 dst_unused:UNUSED_PRESERVE src0_sel:DWORD
	v_cvt_u32_f32_sdwa v169, v101 dst_sel:BYTE_3 dst_unused:UNUSED_PRESERVE src0_sel:DWORD
	v_add_u32_e32 v141, 0x18000, v140
	global_store_dwordx4 v141, v[166:169], s[20:21]
	v_pk_mul_f32 v[94:95], v[94:95], v[160:161]
	v_pk_mul_f32 v[96:97], v[96:97], v[160:161]
	v_pk_mul_f32 v[90:91], v[90:91], v[160:161]
	v_pk_mul_f32 v[92:93], v[92:93], v[160:161]
	v_pk_mul_f32 v[86:87], v[86:87], v[160:161]
	v_pk_mul_f32 v[88:89], v[88:89], v[160:161]
	v_pk_mul_f32 v[82:83], v[82:83], v[160:161]
	v_pk_mul_f32 v[84:85], v[84:85], v[160:161]
	v_exp_f32_e32 v94, v94
	v_exp_f32_e32 v95, v95
	v_exp_f32_e32 v96, v96
	v_exp_f32_e32 v97, v97
	v_exp_f32_e32 v90, v90
	v_exp_f32_e32 v91, v91
	v_exp_f32_e32 v92, v92
	v_exp_f32_e32 v93, v93
	v_exp_f32_e32 v86, v86
	v_exp_f32_e32 v87, v87
	v_exp_f32_e32 v88, v88
	v_exp_f32_e32 v89, v89
	v_exp_f32_e32 v82, v82
	v_exp_f32_e32 v83, v83
	v_exp_f32_e32 v84, v84
	v_exp_f32_e32 v85, v85
	v_pk_add_f32 v[94:95], v[94:95], 1.0 op_sel_hi:[1,0]
	v_pk_add_f32 v[96:97], v[96:97], 1.0 op_sel_hi:[1,0]
	v_pk_add_f32 v[90:91], v[90:91], 1.0 op_sel_hi:[1,0]
	v_pk_add_f32 v[92:93], v[92:93], 1.0 op_sel_hi:[1,0]
	v_pk_add_f32 v[86:87], v[86:87], 1.0 op_sel_hi:[1,0]
	v_pk_add_f32 v[88:89], v[88:89], 1.0 op_sel_hi:[1,0]
	v_pk_add_f32 v[82:83], v[82:83], 1.0 op_sel_hi:[1,0]
	v_pk_add_f32 v[84:85], v[84:85], 1.0 op_sel_hi:[1,0]
	v_rcp_f32_e32 v94, v94
	v_rcp_f32_e32 v95, v95
	v_rcp_f32_e32 v96, v96
	v_rcp_f32_e32 v97, v97
	v_rcp_f32_e32 v90, v90
	v_rcp_f32_e32 v91, v91
	v_rcp_f32_e32 v92, v92
	v_rcp_f32_e32 v93, v93
	v_rcp_f32_e32 v86, v86
	v_rcp_f32_e32 v87, v87
	v_rcp_f32_e32 v88, v88
	v_rcp_f32_e32 v89, v89
	v_rcp_f32_e32 v82, v82
	v_rcp_f32_e32 v83, v83
	v_rcp_f32_e32 v84, v84
	v_rcp_f32_e32 v85, v85
	v_pk_fma_f32 v[94:95], v[94:95], v[162:163], v[164:165]
	v_pk_fma_f32 v[96:97], v[96:97], v[162:163], v[164:165]
	v_pk_fma_f32 v[90:91], v[90:91], v[162:163], v[164:165]
	v_pk_fma_f32 v[92:93], v[92:93], v[162:163], v[164:165]
	v_pk_fma_f32 v[86:87], v[86:87], v[162:163], v[164:165]
	v_pk_fma_f32 v[88:89], v[88:89], v[162:163], v[164:165]
	v_pk_fma_f32 v[82:83], v[82:83], v[162:163], v[164:165]
	v_pk_fma_f32 v[84:85], v[84:85], v[162:163], v[164:165]
	v_max_f32_e32 v94, 1.0, v94
	v_max_f32_e32 v95, 1.0, v95
	v_max_f32_e32 v96, 1.0, v96
	v_max_f32_e32 v97, 1.0, v97
	v_max_f32_e32 v90, 1.0, v90
	v_max_f32_e32 v91, 1.0, v91
	v_max_f32_e32 v92, 1.0, v92
	v_max_f32_e32 v93, 1.0, v93
	v_max_f32_e32 v86, 1.0, v86
	v_max_f32_e32 v87, 1.0, v87
	v_max_f32_e32 v88, 1.0, v88
	v_max_f32_e32 v89, 1.0, v89
	v_max_f32_e32 v82, 1.0, v82
	v_max_f32_e32 v83, 1.0, v83
	v_max_f32_e32 v84, 1.0, v84
	v_max_f32_e32 v85, 1.0, v85
	v_cvt_u32_f32_e32 v154, v94
	v_cvt_u32_f32_e32 v155, v90
	v_cvt_u32_f32_e32 v156, v86
	v_cvt_u32_f32_e32 v157, v82
	v_cvt_u32_f32_sdwa v154, v95 dst_sel:BYTE_1 dst_unused:UNUSED_PRESERVE src0_sel:DWORD
	v_cvt_u32_f32_sdwa v155, v91 dst_sel:BYTE_1 dst_unused:UNUSED_PRESERVE src0_sel:DWORD
	v_cvt_u32_f32_sdwa v156, v87 dst_sel:BYTE_1 dst_unused:UNUSED_PRESERVE src0_sel:DWORD
	v_cvt_u32_f32_sdwa v157, v83 dst_sel:BYTE_1 dst_unused:UNUSED_PRESERVE src0_sel:DWORD
	v_cvt_u32_f32_sdwa v154, v96 dst_sel:BYTE_2 dst_unused:UNUSED_PRESERVE src0_sel:DWORD
	v_cvt_u32_f32_sdwa v155, v92 dst_sel:BYTE_2 dst_unused:UNUSED_PRESERVE src0_sel:DWORD
	v_cvt_u32_f32_sdwa v156, v88 dst_sel:BYTE_2 dst_unused:UNUSED_PRESERVE src0_sel:DWORD
	v_cvt_u32_f32_sdwa v157, v84 dst_sel:BYTE_2 dst_unused:UNUSED_PRESERVE src0_sel:DWORD
	v_cvt_u32_f32_sdwa v154, v97 dst_sel:BYTE_3 dst_unused:UNUSED_PRESERVE src0_sel:DWORD
	v_cvt_u32_f32_sdwa v155, v93 dst_sel:BYTE_3 dst_unused:UNUSED_PRESERVE src0_sel:DWORD
	v_cvt_u32_f32_sdwa v156, v89 dst_sel:BYTE_3 dst_unused:UNUSED_PRESERVE src0_sel:DWORD
	v_cvt_u32_f32_sdwa v157, v85 dst_sel:BYTE_3 dst_unused:UNUSED_PRESERVE src0_sel:DWORD
	v_add_u32_e32 v142, 0x30000, v140
	global_store_dwordx4 v142, v[154:157], s[20:21]
	v_pk_mul_f32 v[78:79], v[78:79], v[160:161]
	v_pk_mul_f32 v[80:81], v[80:81], v[160:161]
	v_pk_mul_f32 v[74:75], v[74:75], v[160:161]
	v_pk_mul_f32 v[76:77], v[76:77], v[160:161]
	v_pk_mul_f32 v[70:71], v[70:71], v[160:161]
	v_pk_mul_f32 v[72:73], v[72:73], v[160:161]
	v_pk_mul_f32 v[66:67], v[66:67], v[160:161]
	v_pk_mul_f32 v[68:69], v[68:69], v[160:161]
	v_exp_f32_e32 v78, v78
	v_exp_f32_e32 v79, v79
	v_exp_f32_e32 v80, v80
	v_exp_f32_e32 v81, v81
	v_exp_f32_e32 v74, v74
	v_exp_f32_e32 v75, v75
	v_exp_f32_e32 v76, v76
	v_exp_f32_e32 v77, v77
	v_exp_f32_e32 v70, v70
	v_exp_f32_e32 v71, v71
	v_exp_f32_e32 v72, v72
	v_exp_f32_e32 v73, v73
	v_exp_f32_e32 v66, v66
	v_exp_f32_e32 v67, v67
	v_exp_f32_e32 v68, v68
	v_exp_f32_e32 v69, v69
	v_pk_add_f32 v[78:79], v[78:79], 1.0 op_sel_hi:[1,0]
	v_pk_add_f32 v[80:81], v[80:81], 1.0 op_sel_hi:[1,0]
	v_pk_add_f32 v[74:75], v[74:75], 1.0 op_sel_hi:[1,0]
	v_pk_add_f32 v[76:77], v[76:77], 1.0 op_sel_hi:[1,0]
	v_pk_add_f32 v[70:71], v[70:71], 1.0 op_sel_hi:[1,0]
	v_pk_add_f32 v[72:73], v[72:73], 1.0 op_sel_hi:[1,0]
	v_pk_add_f32 v[66:67], v[66:67], 1.0 op_sel_hi:[1,0]
	v_pk_add_f32 v[68:69], v[68:69], 1.0 op_sel_hi:[1,0]
	v_rcp_f32_e32 v78, v78
	v_rcp_f32_e32 v79, v79
	v_rcp_f32_e32 v80, v80
	v_rcp_f32_e32 v81, v81
	v_rcp_f32_e32 v74, v74
	v_rcp_f32_e32 v75, v75
	v_rcp_f32_e32 v76, v76
	v_rcp_f32_e32 v77, v77
	v_rcp_f32_e32 v70, v70
	v_rcp_f32_e32 v71, v71
	v_rcp_f32_e32 v72, v72
	v_rcp_f32_e32 v73, v73
	v_rcp_f32_e32 v66, v66
	v_rcp_f32_e32 v67, v67
	v_rcp_f32_e32 v68, v68
	v_rcp_f32_e32 v69, v69
	v_pk_fma_f32 v[78:79], v[78:79], v[162:163], v[164:165]
	v_pk_fma_f32 v[80:81], v[80:81], v[162:163], v[164:165]
	v_pk_fma_f32 v[74:75], v[74:75], v[162:163], v[164:165]
	v_pk_fma_f32 v[76:77], v[76:77], v[162:163], v[164:165]
	v_pk_fma_f32 v[70:71], v[70:71], v[162:163], v[164:165]
	v_pk_fma_f32 v[72:73], v[72:73], v[162:163], v[164:165]
	v_pk_fma_f32 v[66:67], v[66:67], v[162:163], v[164:165]
	v_pk_fma_f32 v[68:69], v[68:69], v[162:163], v[164:165]
	v_max_f32_e32 v78, 1.0, v78
	v_max_f32_e32 v79, 1.0, v79
	v_max_f32_e32 v80, 1.0, v80
	v_max_f32_e32 v81, 1.0, v81
	v_max_f32_e32 v74, 1.0, v74
	v_max_f32_e32 v75, 1.0, v75
	v_max_f32_e32 v76, 1.0, v76
	v_max_f32_e32 v77, 1.0, v77
	v_max_f32_e32 v70, 1.0, v70
	v_max_f32_e32 v71, 1.0, v71
	v_max_f32_e32 v72, 1.0, v72
	v_max_f32_e32 v73, 1.0, v73
	v_max_f32_e32 v66, 1.0, v66
	v_max_f32_e32 v67, 1.0, v67
	v_max_f32_e32 v68, 1.0, v68
	v_max_f32_e32 v69, 1.0, v69
	v_cvt_u32_f32_e32 v166, v78
	v_cvt_u32_f32_e32 v167, v74
	v_cvt_u32_f32_e32 v168, v70
	v_cvt_u32_f32_e32 v169, v66
	v_cvt_u32_f32_sdwa v166, v79 dst_sel:BYTE_1 dst_unused:UNUSED_PRESERVE src0_sel:DWORD
	v_cvt_u32_f32_sdwa v167, v75 dst_sel:BYTE_1 dst_unused:UNUSED_PRESERVE src0_sel:DWORD
	v_cvt_u32_f32_sdwa v168, v71 dst_sel:BYTE_1 dst_unused:UNUSED_PRESERVE src0_sel:DWORD
	v_cvt_u32_f32_sdwa v169, v67 dst_sel:BYTE_1 dst_unused:UNUSED_PRESERVE src0_sel:DWORD
	v_cvt_u32_f32_sdwa v166, v80 dst_sel:BYTE_2 dst_unused:UNUSED_PRESERVE src0_sel:DWORD
	v_cvt_u32_f32_sdwa v167, v76 dst_sel:BYTE_2 dst_unused:UNUSED_PRESERVE src0_sel:DWORD
	v_cvt_u32_f32_sdwa v168, v72 dst_sel:BYTE_2 dst_unused:UNUSED_PRESERVE src0_sel:DWORD
	v_cvt_u32_f32_sdwa v169, v68 dst_sel:BYTE_2 dst_unused:UNUSED_PRESERVE src0_sel:DWORD
	v_cvt_u32_f32_sdwa v166, v81 dst_sel:BYTE_3 dst_unused:UNUSED_PRESERVE src0_sel:DWORD
	v_cvt_u32_f32_sdwa v167, v77 dst_sel:BYTE_3 dst_unused:UNUSED_PRESERVE src0_sel:DWORD
	v_cvt_u32_f32_sdwa v168, v73 dst_sel:BYTE_3 dst_unused:UNUSED_PRESERVE src0_sel:DWORD
	v_cvt_u32_f32_sdwa v169, v69 dst_sel:BYTE_3 dst_unused:UNUSED_PRESERVE src0_sel:DWORD
	v_add_u32_e32 v141, 0x48000, v140
	global_store_dwordx4 v141, v[166:169], s[20:21]
	v_pk_mul_f32 v[62:63], v[62:63], v[160:161]
	v_pk_mul_f32 v[64:65], v[64:65], v[160:161]
	v_pk_mul_f32 v[58:59], v[58:59], v[160:161]
	v_pk_mul_f32 v[60:61], v[60:61], v[160:161]
	v_pk_mul_f32 v[54:55], v[54:55], v[160:161]
	v_pk_mul_f32 v[56:57], v[56:57], v[160:161]
	v_pk_mul_f32 v[50:51], v[50:51], v[160:161]
	v_pk_mul_f32 v[52:53], v[52:53], v[160:161]
	v_exp_f32_e32 v62, v62
	v_exp_f32_e32 v63, v63
	v_exp_f32_e32 v64, v64
	v_exp_f32_e32 v65, v65
	v_exp_f32_e32 v58, v58
	v_exp_f32_e32 v59, v59
	v_exp_f32_e32 v60, v60
	v_exp_f32_e32 v61, v61
	v_exp_f32_e32 v54, v54
	v_exp_f32_e32 v55, v55
	v_exp_f32_e32 v56, v56
	v_exp_f32_e32 v57, v57
	v_exp_f32_e32 v50, v50
	v_exp_f32_e32 v51, v51
	v_exp_f32_e32 v52, v52
	v_exp_f32_e32 v53, v53
	v_pk_add_f32 v[62:63], v[62:63], 1.0 op_sel_hi:[1,0]
	v_pk_add_f32 v[64:65], v[64:65], 1.0 op_sel_hi:[1,0]
	v_pk_add_f32 v[58:59], v[58:59], 1.0 op_sel_hi:[1,0]
	v_pk_add_f32 v[60:61], v[60:61], 1.0 op_sel_hi:[1,0]
	v_pk_add_f32 v[54:55], v[54:55], 1.0 op_sel_hi:[1,0]
	v_pk_add_f32 v[56:57], v[56:57], 1.0 op_sel_hi:[1,0]
	v_pk_add_f32 v[50:51], v[50:51], 1.0 op_sel_hi:[1,0]
	v_pk_add_f32 v[52:53], v[52:53], 1.0 op_sel_hi:[1,0]
	v_rcp_f32_e32 v62, v62
	v_rcp_f32_e32 v63, v63
	v_rcp_f32_e32 v64, v64
	v_rcp_f32_e32 v65, v65
	v_rcp_f32_e32 v58, v58
	v_rcp_f32_e32 v59, v59
	v_rcp_f32_e32 v60, v60
	v_rcp_f32_e32 v61, v61
	v_rcp_f32_e32 v54, v54
	v_rcp_f32_e32 v55, v55
	v_rcp_f32_e32 v56, v56
	v_rcp_f32_e32 v57, v57
	v_rcp_f32_e32 v50, v50
	v_rcp_f32_e32 v51, v51
	v_rcp_f32_e32 v52, v52
	v_rcp_f32_e32 v53, v53
	v_pk_fma_f32 v[62:63], v[62:63], v[162:163], v[164:165]
	v_pk_fma_f32 v[64:65], v[64:65], v[162:163], v[164:165]
	v_pk_fma_f32 v[58:59], v[58:59], v[162:163], v[164:165]
	v_pk_fma_f32 v[60:61], v[60:61], v[162:163], v[164:165]
	v_pk_fma_f32 v[54:55], v[54:55], v[162:163], v[164:165]
	v_pk_fma_f32 v[56:57], v[56:57], v[162:163], v[164:165]
	v_pk_fma_f32 v[50:51], v[50:51], v[162:163], v[164:165]
	v_pk_fma_f32 v[52:53], v[52:53], v[162:163], v[164:165]
	v_max_f32_e32 v62, 1.0, v62
	v_max_f32_e32 v63, 1.0, v63
	v_max_f32_e32 v64, 1.0, v64
	v_max_f32_e32 v65, 1.0, v65
	v_max_f32_e32 v58, 1.0, v58
	v_max_f32_e32 v59, 1.0, v59
	v_max_f32_e32 v60, 1.0, v60
	v_max_f32_e32 v61, 1.0, v61
	v_max_f32_e32 v54, 1.0, v54
	v_max_f32_e32 v55, 1.0, v55
	v_max_f32_e32 v56, 1.0, v56
	v_max_f32_e32 v57, 1.0, v57
	v_max_f32_e32 v50, 1.0, v50
	v_max_f32_e32 v51, 1.0, v51
	v_max_f32_e32 v52, 1.0, v52
	v_max_f32_e32 v53, 1.0, v53
	v_cvt_u32_f32_e32 v154, v62
	v_cvt_u32_f32_e32 v155, v58
	v_cvt_u32_f32_e32 v156, v54
	v_cvt_u32_f32_e32 v157, v50
	v_cvt_u32_f32_sdwa v154, v63 dst_sel:BYTE_1 dst_unused:UNUSED_PRESERVE src0_sel:DWORD
	v_cvt_u32_f32_sdwa v155, v59 dst_sel:BYTE_1 dst_unused:UNUSED_PRESERVE src0_sel:DWORD
	v_cvt_u32_f32_sdwa v156, v55 dst_sel:BYTE_1 dst_unused:UNUSED_PRESERVE src0_sel:DWORD
	v_cvt_u32_f32_sdwa v157, v51 dst_sel:BYTE_1 dst_unused:UNUSED_PRESERVE src0_sel:DWORD
	v_cvt_u32_f32_sdwa v154, v64 dst_sel:BYTE_2 dst_unused:UNUSED_PRESERVE src0_sel:DWORD
	v_cvt_u32_f32_sdwa v155, v60 dst_sel:BYTE_2 dst_unused:UNUSED_PRESERVE src0_sel:DWORD
	v_cvt_u32_f32_sdwa v156, v56 dst_sel:BYTE_2 dst_unused:UNUSED_PRESERVE src0_sel:DWORD
	v_cvt_u32_f32_sdwa v157, v52 dst_sel:BYTE_2 dst_unused:UNUSED_PRESERVE src0_sel:DWORD
	v_cvt_u32_f32_sdwa v154, v65 dst_sel:BYTE_3 dst_unused:UNUSED_PRESERVE src0_sel:DWORD
	v_cvt_u32_f32_sdwa v155, v61 dst_sel:BYTE_3 dst_unused:UNUSED_PRESERVE src0_sel:DWORD
	v_cvt_u32_f32_sdwa v156, v57 dst_sel:BYTE_3 dst_unused:UNUSED_PRESERVE src0_sel:DWORD
	v_cvt_u32_f32_sdwa v157, v53 dst_sel:BYTE_3 dst_unused:UNUSED_PRESERVE src0_sel:DWORD
	v_add_u32_e32 v142, 0xc0000, v140
	global_store_dwordx4 v142, v[154:157], s[20:21]
	v_pk_mul_f32 v[46:47], v[46:47], v[160:161]
	v_pk_mul_f32 v[48:49], v[48:49], v[160:161]
	v_pk_mul_f32 v[42:43], v[42:43], v[160:161]
	v_pk_mul_f32 v[44:45], v[44:45], v[160:161]
	v_pk_mul_f32 v[38:39], v[38:39], v[160:161]
	v_pk_mul_f32 v[40:41], v[40:41], v[160:161]
	v_pk_mul_f32 v[34:35], v[34:35], v[160:161]
	v_pk_mul_f32 v[36:37], v[36:37], v[160:161]
	v_exp_f32_e32 v46, v46
	v_exp_f32_e32 v47, v47
	v_exp_f32_e32 v48, v48
	v_exp_f32_e32 v49, v49
	v_exp_f32_e32 v42, v42
	v_exp_f32_e32 v43, v43
	v_exp_f32_e32 v44, v44
	v_exp_f32_e32 v45, v45
	v_exp_f32_e32 v38, v38
	v_exp_f32_e32 v39, v39
	v_exp_f32_e32 v40, v40
	v_exp_f32_e32 v41, v41
	v_exp_f32_e32 v34, v34
	v_exp_f32_e32 v35, v35
	v_exp_f32_e32 v36, v36
	v_exp_f32_e32 v37, v37
	v_pk_add_f32 v[46:47], v[46:47], 1.0 op_sel_hi:[1,0]
	v_pk_add_f32 v[48:49], v[48:49], 1.0 op_sel_hi:[1,0]
	v_pk_add_f32 v[42:43], v[42:43], 1.0 op_sel_hi:[1,0]
	v_pk_add_f32 v[44:45], v[44:45], 1.0 op_sel_hi:[1,0]
	v_pk_add_f32 v[38:39], v[38:39], 1.0 op_sel_hi:[1,0]
	v_pk_add_f32 v[40:41], v[40:41], 1.0 op_sel_hi:[1,0]
	v_pk_add_f32 v[34:35], v[34:35], 1.0 op_sel_hi:[1,0]
	v_pk_add_f32 v[36:37], v[36:37], 1.0 op_sel_hi:[1,0]
	v_rcp_f32_e32 v46, v46
	v_rcp_f32_e32 v47, v47
	v_rcp_f32_e32 v48, v48
	v_rcp_f32_e32 v49, v49
	v_rcp_f32_e32 v42, v42
	v_rcp_f32_e32 v43, v43
	v_rcp_f32_e32 v44, v44
	v_rcp_f32_e32 v45, v45
	v_rcp_f32_e32 v38, v38
	v_rcp_f32_e32 v39, v39
	v_rcp_f32_e32 v40, v40
	v_rcp_f32_e32 v41, v41
	v_rcp_f32_e32 v34, v34
	v_rcp_f32_e32 v35, v35
	v_rcp_f32_e32 v36, v36
	v_rcp_f32_e32 v37, v37
	v_pk_fma_f32 v[46:47], v[46:47], v[162:163], v[164:165]
	v_pk_fma_f32 v[48:49], v[48:49], v[162:163], v[164:165]
	v_pk_fma_f32 v[42:43], v[42:43], v[162:163], v[164:165]
	v_pk_fma_f32 v[44:45], v[44:45], v[162:163], v[164:165]
	v_pk_fma_f32 v[38:39], v[38:39], v[162:163], v[164:165]
	v_pk_fma_f32 v[40:41], v[40:41], v[162:163], v[164:165]
	v_pk_fma_f32 v[34:35], v[34:35], v[162:163], v[164:165]
	v_pk_fma_f32 v[36:37], v[36:37], v[162:163], v[164:165]
	v_max_f32_e32 v46, 1.0, v46
	v_max_f32_e32 v47, 1.0, v47
	v_max_f32_e32 v48, 1.0, v48
	v_max_f32_e32 v49, 1.0, v49
	v_max_f32_e32 v42, 1.0, v42
	v_max_f32_e32 v43, 1.0, v43
	v_max_f32_e32 v44, 1.0, v44
	v_max_f32_e32 v45, 1.0, v45
	v_max_f32_e32 v38, 1.0, v38
	v_max_f32_e32 v39, 1.0, v39
	v_max_f32_e32 v40, 1.0, v40
	v_max_f32_e32 v41, 1.0, v41
	v_max_f32_e32 v34, 1.0, v34
	v_max_f32_e32 v35, 1.0, v35
	v_max_f32_e32 v36, 1.0, v36
	v_max_f32_e32 v37, 1.0, v37
	v_cvt_u32_f32_e32 v166, v46
	v_cvt_u32_f32_e32 v167, v42
	v_cvt_u32_f32_e32 v168, v38
	v_cvt_u32_f32_e32 v169, v34
	v_cvt_u32_f32_sdwa v166, v47 dst_sel:BYTE_1 dst_unused:UNUSED_PRESERVE src0_sel:DWORD
	v_cvt_u32_f32_sdwa v167, v43 dst_sel:BYTE_1 dst_unused:UNUSED_PRESERVE src0_sel:DWORD
	v_cvt_u32_f32_sdwa v168, v39 dst_sel:BYTE_1 dst_unused:UNUSED_PRESERVE src0_sel:DWORD
	v_cvt_u32_f32_sdwa v169, v35 dst_sel:BYTE_1 dst_unused:UNUSED_PRESERVE src0_sel:DWORD
	v_cvt_u32_f32_sdwa v166, v48 dst_sel:BYTE_2 dst_unused:UNUSED_PRESERVE src0_sel:DWORD
	v_cvt_u32_f32_sdwa v167, v44 dst_sel:BYTE_2 dst_unused:UNUSED_PRESERVE src0_sel:DWORD
	v_cvt_u32_f32_sdwa v168, v40 dst_sel:BYTE_2 dst_unused:UNUSED_PRESERVE src0_sel:DWORD
	v_cvt_u32_f32_sdwa v169, v36 dst_sel:BYTE_2 dst_unused:UNUSED_PRESERVE src0_sel:DWORD
	v_cvt_u32_f32_sdwa v166, v49 dst_sel:BYTE_3 dst_unused:UNUSED_PRESERVE src0_sel:DWORD
	v_cvt_u32_f32_sdwa v167, v45 dst_sel:BYTE_3 dst_unused:UNUSED_PRESERVE src0_sel:DWORD
	v_cvt_u32_f32_sdwa v168, v41 dst_sel:BYTE_3 dst_unused:UNUSED_PRESERVE src0_sel:DWORD
	v_cvt_u32_f32_sdwa v169, v37 dst_sel:BYTE_3 dst_unused:UNUSED_PRESERVE src0_sel:DWORD
	v_add_u32_e32 v141, 0xd8000, v140
	global_store_dwordx4 v141, v[166:169], s[20:21]
	v_pk_mul_f32 v[30:31], v[30:31], v[160:161]
	v_pk_mul_f32 v[32:33], v[32:33], v[160:161]
	v_pk_mul_f32 v[26:27], v[26:27], v[160:161]
	v_pk_mul_f32 v[28:29], v[28:29], v[160:161]
	v_pk_mul_f32 v[22:23], v[22:23], v[160:161]
	v_pk_mul_f32 v[24:25], v[24:25], v[160:161]
	v_pk_mul_f32 v[18:19], v[18:19], v[160:161]
	v_pk_mul_f32 v[20:21], v[20:21], v[160:161]
	v_exp_f32_e32 v30, v30
	v_exp_f32_e32 v31, v31
	v_exp_f32_e32 v32, v32
	v_exp_f32_e32 v33, v33
	v_exp_f32_e32 v26, v26
	v_exp_f32_e32 v27, v27
	v_exp_f32_e32 v28, v28
	v_exp_f32_e32 v29, v29
	v_exp_f32_e32 v22, v22
	v_exp_f32_e32 v23, v23
	v_exp_f32_e32 v24, v24
	v_exp_f32_e32 v25, v25
	v_exp_f32_e32 v18, v18
	v_exp_f32_e32 v19, v19
	v_exp_f32_e32 v20, v20
	v_exp_f32_e32 v21, v21
	v_pk_add_f32 v[30:31], v[30:31], 1.0 op_sel_hi:[1,0]
	v_pk_add_f32 v[32:33], v[32:33], 1.0 op_sel_hi:[1,0]
	v_pk_add_f32 v[26:27], v[26:27], 1.0 op_sel_hi:[1,0]
	v_pk_add_f32 v[28:29], v[28:29], 1.0 op_sel_hi:[1,0]
	v_pk_add_f32 v[22:23], v[22:23], 1.0 op_sel_hi:[1,0]
	v_pk_add_f32 v[24:25], v[24:25], 1.0 op_sel_hi:[1,0]
	v_pk_add_f32 v[18:19], v[18:19], 1.0 op_sel_hi:[1,0]
	v_pk_add_f32 v[20:21], v[20:21], 1.0 op_sel_hi:[1,0]
	v_rcp_f32_e32 v30, v30
	v_rcp_f32_e32 v31, v31
	v_rcp_f32_e32 v32, v32
	v_rcp_f32_e32 v33, v33
	v_rcp_f32_e32 v26, v26
	v_rcp_f32_e32 v27, v27
	v_rcp_f32_e32 v28, v28
	v_rcp_f32_e32 v29, v29
	v_rcp_f32_e32 v22, v22
	v_rcp_f32_e32 v23, v23
	v_rcp_f32_e32 v24, v24
	v_rcp_f32_e32 v25, v25
	v_rcp_f32_e32 v18, v18
	v_rcp_f32_e32 v19, v19
	v_rcp_f32_e32 v20, v20
	v_rcp_f32_e32 v21, v21
	v_pk_fma_f32 v[30:31], v[30:31], v[162:163], v[164:165]
	v_pk_fma_f32 v[32:33], v[32:33], v[162:163], v[164:165]
	v_pk_fma_f32 v[26:27], v[26:27], v[162:163], v[164:165]
	v_pk_fma_f32 v[28:29], v[28:29], v[162:163], v[164:165]
	v_pk_fma_f32 v[22:23], v[22:23], v[162:163], v[164:165]
	v_pk_fma_f32 v[24:25], v[24:25], v[162:163], v[164:165]
	v_pk_fma_f32 v[18:19], v[18:19], v[162:163], v[164:165]
	v_pk_fma_f32 v[20:21], v[20:21], v[162:163], v[164:165]
	v_max_f32_e32 v30, 1.0, v30
	v_max_f32_e32 v31, 1.0, v31
	v_max_f32_e32 v32, 1.0, v32
	v_max_f32_e32 v33, 1.0, v33
	v_max_f32_e32 v26, 1.0, v26
	v_max_f32_e32 v27, 1.0, v27
	v_max_f32_e32 v28, 1.0, v28
	v_max_f32_e32 v29, 1.0, v29
	v_max_f32_e32 v22, 1.0, v22
	v_max_f32_e32 v23, 1.0, v23
	v_max_f32_e32 v24, 1.0, v24
	v_max_f32_e32 v25, 1.0, v25
	v_max_f32_e32 v18, 1.0, v18
	v_max_f32_e32 v19, 1.0, v19
	v_max_f32_e32 v20, 1.0, v20
	v_max_f32_e32 v21, 1.0, v21
	v_cvt_u32_f32_e32 v154, v30
	v_cvt_u32_f32_e32 v155, v26
	v_cvt_u32_f32_e32 v156, v22
	v_cvt_u32_f32_e32 v157, v18
	v_cvt_u32_f32_sdwa v154, v31 dst_sel:BYTE_1 dst_unused:UNUSED_PRESERVE src0_sel:DWORD
	v_cvt_u32_f32_sdwa v155, v27 dst_sel:BYTE_1 dst_unused:UNUSED_PRESERVE src0_sel:DWORD
	v_cvt_u32_f32_sdwa v156, v23 dst_sel:BYTE_1 dst_unused:UNUSED_PRESERVE src0_sel:DWORD
	v_cvt_u32_f32_sdwa v157, v19 dst_sel:BYTE_1 dst_unused:UNUSED_PRESERVE src0_sel:DWORD
	v_cvt_u32_f32_sdwa v154, v32 dst_sel:BYTE_2 dst_unused:UNUSED_PRESERVE src0_sel:DWORD
	v_cvt_u32_f32_sdwa v155, v28 dst_sel:BYTE_2 dst_unused:UNUSED_PRESERVE src0_sel:DWORD
	v_cvt_u32_f32_sdwa v156, v24 dst_sel:BYTE_2 dst_unused:UNUSED_PRESERVE src0_sel:DWORD
	v_cvt_u32_f32_sdwa v157, v20 dst_sel:BYTE_2 dst_unused:UNUSED_PRESERVE src0_sel:DWORD
	v_cvt_u32_f32_sdwa v154, v33 dst_sel:BYTE_3 dst_unused:UNUSED_PRESERVE src0_sel:DWORD
	v_cvt_u32_f32_sdwa v155, v29 dst_sel:BYTE_3 dst_unused:UNUSED_PRESERVE src0_sel:DWORD
	v_cvt_u32_f32_sdwa v156, v25 dst_sel:BYTE_3 dst_unused:UNUSED_PRESERVE src0_sel:DWORD
	v_cvt_u32_f32_sdwa v157, v21 dst_sel:BYTE_3 dst_unused:UNUSED_PRESERVE src0_sel:DWORD
	v_add_u32_e32 v142, 0xf0000, v140
	global_store_dwordx4 v142, v[154:157], s[20:21]
	v_pk_mul_f32 v[14:15], v[14:15], v[160:161]
	v_pk_mul_f32 v[16:17], v[16:17], v[160:161]
	v_pk_mul_f32 v[10:11], v[10:11], v[160:161]
	v_pk_mul_f32 v[12:13], v[12:13], v[160:161]
	v_pk_mul_f32 v[6:7], v[6:7], v[160:161]
	v_pk_mul_f32 v[8:9], v[8:9], v[160:161]
	v_pk_mul_f32 v[2:3], v[2:3], v[160:161]
	v_pk_mul_f32 v[4:5], v[4:5], v[160:161]
	v_exp_f32_e32 v14, v14
	v_exp_f32_e32 v15, v15
	v_exp_f32_e32 v16, v16
	v_exp_f32_e32 v17, v17
	v_exp_f32_e32 v10, v10
	v_exp_f32_e32 v11, v11
	v_exp_f32_e32 v12, v12
	v_exp_f32_e32 v13, v13
	v_exp_f32_e32 v6, v6
	v_exp_f32_e32 v7, v7
	v_exp_f32_e32 v8, v8
	v_exp_f32_e32 v9, v9
	v_exp_f32_e32 v2, v2
	v_exp_f32_e32 v3, v3
	v_exp_f32_e32 v4, v4
	v_exp_f32_e32 v5, v5
	v_pk_add_f32 v[14:15], v[14:15], 1.0 op_sel_hi:[1,0]
	v_pk_add_f32 v[16:17], v[16:17], 1.0 op_sel_hi:[1,0]
	v_pk_add_f32 v[10:11], v[10:11], 1.0 op_sel_hi:[1,0]
	v_pk_add_f32 v[12:13], v[12:13], 1.0 op_sel_hi:[1,0]
	v_pk_add_f32 v[6:7], v[6:7], 1.0 op_sel_hi:[1,0]
	v_pk_add_f32 v[8:9], v[8:9], 1.0 op_sel_hi:[1,0]
	v_pk_add_f32 v[2:3], v[2:3], 1.0 op_sel_hi:[1,0]
	v_pk_add_f32 v[4:5], v[4:5], 1.0 op_sel_hi:[1,0]
	v_rcp_f32_e32 v14, v14
	v_rcp_f32_e32 v15, v15
	v_rcp_f32_e32 v16, v16
	v_rcp_f32_e32 v17, v17
	v_rcp_f32_e32 v10, v10
	v_rcp_f32_e32 v11, v11
	v_rcp_f32_e32 v12, v12
	v_rcp_f32_e32 v13, v13
	v_rcp_f32_e32 v6, v6
	v_rcp_f32_e32 v7, v7
	v_rcp_f32_e32 v8, v8
	v_rcp_f32_e32 v9, v9
	v_rcp_f32_e32 v2, v2
	v_rcp_f32_e32 v3, v3
	v_rcp_f32_e32 v4, v4
	v_rcp_f32_e32 v5, v5
	v_pk_fma_f32 v[14:15], v[14:15], v[162:163], v[164:165]
	v_pk_fma_f32 v[16:17], v[16:17], v[162:163], v[164:165]
	v_pk_fma_f32 v[10:11], v[10:11], v[162:163], v[164:165]
	v_pk_fma_f32 v[12:13], v[12:13], v[162:163], v[164:165]
	v_pk_fma_f32 v[6:7], v[6:7], v[162:163], v[164:165]
	v_pk_fma_f32 v[8:9], v[8:9], v[162:163], v[164:165]
	v_pk_fma_f32 v[2:3], v[2:3], v[162:163], v[164:165]
	v_pk_fma_f32 v[4:5], v[4:5], v[162:163], v[164:165]
	v_max_f32_e32 v14, 1.0, v14
	v_max_f32_e32 v15, 1.0, v15
	v_max_f32_e32 v16, 1.0, v16
	v_max_f32_e32 v17, 1.0, v17
	v_max_f32_e32 v10, 1.0, v10
	v_max_f32_e32 v11, 1.0, v11
	v_max_f32_e32 v12, 1.0, v12
	v_max_f32_e32 v13, 1.0, v13
	v_max_f32_e32 v6, 1.0, v6
	v_max_f32_e32 v7, 1.0, v7
	v_max_f32_e32 v8, 1.0, v8
	v_max_f32_e32 v9, 1.0, v9
	v_max_f32_e32 v2, 1.0, v2
	v_max_f32_e32 v3, 1.0, v3
	v_max_f32_e32 v4, 1.0, v4
	v_max_f32_e32 v5, 1.0, v5
	v_cvt_u32_f32_e32 v166, v14
	v_cvt_u32_f32_e32 v167, v10
	v_cvt_u32_f32_e32 v168, v6
	v_cvt_u32_f32_e32 v169, v2
	v_cvt_u32_f32_sdwa v166, v15 dst_sel:BYTE_1 dst_unused:UNUSED_PRESERVE src0_sel:DWORD
	v_cvt_u32_f32_sdwa v167, v11 dst_sel:BYTE_1 dst_unused:UNUSED_PRESERVE src0_sel:DWORD
	v_cvt_u32_f32_sdwa v168, v7 dst_sel:BYTE_1 dst_unused:UNUSED_PRESERVE src0_sel:DWORD
	v_cvt_u32_f32_sdwa v169, v3 dst_sel:BYTE_1 dst_unused:UNUSED_PRESERVE src0_sel:DWORD
	v_cvt_u32_f32_sdwa v166, v16 dst_sel:BYTE_2 dst_unused:UNUSED_PRESERVE src0_sel:DWORD
	v_cvt_u32_f32_sdwa v167, v12 dst_sel:BYTE_2 dst_unused:UNUSED_PRESERVE src0_sel:DWORD
	v_cvt_u32_f32_sdwa v168, v8 dst_sel:BYTE_2 dst_unused:UNUSED_PRESERVE src0_sel:DWORD
	v_cvt_u32_f32_sdwa v169, v4 dst_sel:BYTE_2 dst_unused:UNUSED_PRESERVE src0_sel:DWORD
	v_cvt_u32_f32_sdwa v166, v17 dst_sel:BYTE_3 dst_unused:UNUSED_PRESERVE src0_sel:DWORD
	v_cvt_u32_f32_sdwa v167, v13 dst_sel:BYTE_3 dst_unused:UNUSED_PRESERVE src0_sel:DWORD
	v_cvt_u32_f32_sdwa v168, v9 dst_sel:BYTE_3 dst_unused:UNUSED_PRESERVE src0_sel:DWORD
	v_cvt_u32_f32_sdwa v169, v5 dst_sel:BYTE_3 dst_unused:UNUSED_PRESERVE src0_sel:DWORD
	v_add_u32_e32 v141, 0x108000, v140
	global_store_dwordx4 v141, v[166:169], s[20:21]
	s_mov_b32 s32, 0
	s_cbranch_execnz .LBB0_94
